# static priority raise for waves 0-3 at level 3 instead of 1 (on top of v76)
# baseline (speedup 1.0000x reference)
_Z3fwd4Args:
	s_mov_b32 s96, s2
	s_load_dwordx4 s[44:47], s[0:1], 0xc8
	s_add_u32 s2, s0, 0xd8
	s_addc_u32 s3, s1, 0
	v_readfirstlane_b32 s10, v0
	v_writelane_b32 v252, s2, 0
	s_nop 1
	v_writelane_b32 v252, s3, 1
	s_movk_i32 s2, 0x200
	v_cmp_gt_u32_e32 vcc, s2, v0
	s_and_saveexec_b64 s[4:5], vcc
	v_lshl_add_u32 v1, v0, 2, 0
	v_add_u32_e32 v1, 0x24c00, v1
	v_mov_b32_e32 v2, 0
	ds_write_b32 v1, v2
	s_or_b64 exec, exec, s[4:5]
	s_lshr_b32 s4, s10, 6
	s_cmp_ge_u32 s4, 4
	s_cbranch_scc1 .Lprio_static_done
	s_setprio 3
